# speedup vs baseline: 1.0552x; 1.0041x over previous
_Z12embed_kernelPKiS0_S0_S0_S0_PKfS2_S2_S2_S2_S2_S2_S2_PKDv8_DF16_PfiS2_S2_PS3_S0_S0_PiS8_S8_P15HIP_vector_typeIiLj2EES8_:
	s_load_dword s3, s[0:1], 0x78
	v_and_b32_e32 v1, 31, v0
	s_mov_b64 s[4:5], -1
	s_waitcnt lgkmcnt(0)
	s_cmp_lt_i32 s2, s3
	s_cbranch_scc1 .LBB1_35
	s_sub_i32 s3, s2, s3
	v_lshl_or_b32 v6, s3, 8, v0
	s_mov_b32 s3, 0xab800
	v_cmp_gt_u32_e32 vcc, s3, v6
	s_and_saveexec_b64 s[4:5], vcc
	s_xor_b64 s[6:7], exec, s[4:5]
	s_cbranch_execz .LBB1_9
	v_lshrrev_b32_e32 v2, 6, v6
	v_mul_u32_u24_e32 v3, 0x2493, v2
	v_sub_u16_sdwa v4, v2, v3 dst_sel:DWORD dst_unused:UNUSED_PAD src0_sel:DWORD src1_sel:WORD_1
	v_lshrrev_b16_e32 v4, 1, v4
	s_load_dwordx2 s[4:5], s[0:1], 0x80
	v_add_u16_sdwa v3, v4, v3 dst_sel:DWORD dst_unused:UNUSED_PAD src0_sel:DWORD src1_sel:WORD_1
	v_lshrrev_b16_e32 v3, 2, v3
	v_mul_lo_u16_e32 v3, 7, v3
	s_mov_b32 s3, 0x24924925
	v_sub_u16_e32 v5, v2, v3
	v_mul_hi_u32 v2, v2, s3
	v_lshl_or_b32 v7, v2, 5, v1
	v_lshlrev_b16_e32 v2, 4, v5
	v_lshrrev_b32_e32 v3, 2, v0
	v_and_or_b32 v10, v3, 8, v2
	s_movk_i32 s3, 0x190
	s_waitcnt lgkmcnt(0)
	v_mov_b64_e32 v[2:3], s[4:5]
	v_mad_u64_u32 v[2:3], s[4:5], v7, s3, v[2:3]
	s_mov_b32 s3, 0xc350
	v_cmp_gt_u32_e32 vcc, s3, v7
	s_movk_i32 s3, 0x64
	v_cmp_gt_u32_e64 s[4:5], s3, v10
	v_mov_b32_e32 v11, 0
	s_and_b64 s[8:9], vcc, s[4:5]
	v_mov_b32_e32 v4, 0
	v_lshlrev_b32_e32 v8, 2, v10
	v_mov_b32_e32 v12, 0
	v_mov_b32_e32 v13, 0
	v_cmp_gt_u16_e64 s[4:5], 6, v5
	s_and_b64 s[10:11], s[4:5], vcc
	v_mov_b32_e32 v5, 0
	v_mov_b32_e32 v9, 0
	v_lshl_add_u64 v[18:19], v[2:3], 0, v[8:9]
	s_mov_b64 s[12:13], exec
	s_and_b64 exec, s[12:13], s[8:9]
	s_cbranch_execz .Lemb_cvt_noa
	global_load_dwordx4 v[20:23], v[18:19], off
.Lemb_cvt_noa:
	s_and_b64 exec, s[12:13], s[10:11]
	s_cbranch_execz .Lemb_cvt_nob
	global_load_dwordx4 v[24:27], v[18:19], off offset:16
.Lemb_cvt_nob:
	s_waitcnt vmcnt(0)
	s_and_b64 exec, s[12:13], s[8:9]
	v_cvt_f16_f32_e32 v11, v20
	v_cvt_f16_f32_e32 v12, v23
	v_cvt_pk_f16_f32 v13, v21, v22
	s_and_b64 exec, s[12:13], s[10:11]
	v_cvt_pk_f16_f32 v4, v24, v25
	v_cvt_pk_f16_f32 v5, v26, v27
	s_mov_b64 exec, s[12:13]
	s_load_dwordx2 s[8:9], s[0:1], 0x90
	s_mov_b32 s3, 0x5040100
	v_perm_b32 v2, v13, v11, s3
	s_movk_i32 s3, 0x60
	v_cmp_eq_u32_e64 s[4:5], s3, v10
	v_alignbit_b32 v3, v12, v13, 16
	s_and_b64 s[10:11], vcc, s[4:5]
	s_and_saveexec_b64 s[4:5], s[10:11]
	s_cbranch_execz .LBB1_8
	s_load_dwordx2 s[10:11], s[0:1], 0x88
	v_lshlrev_b32_e32 v4, 2, v7
	s_waitcnt lgkmcnt(0)
	global_load_dword v4, v4, s[10:11]
	s_waitcnt vmcnt(0)
	v_cvt_f16_f32_e32 v7, v4
	v_cvt_f32_f16_e32 v7, v7
	v_sub_f32_e32 v7, v4, v7
	v_cvt_pk_f16_f32 v4, v4, v7

_Z11pool_kernelPKfPKiPDF16_:
	s_load_dwordx2 s[4:5], s[0:1], 0x8
	v_lshrrev_b32_e32 v12, 7, v0
	v_lshl_or_b32 v6, s2, 1, v12
	v_ashrrev_i32_e32 v7, 31, v6
	v_and_b32_e32 v10, 31, v0
	s_waitcnt lgkmcnt(0)
	v_lshl_add_u64 v[2:3], v[6:7], 2, s[4:5]
	global_load_dwordx2 v[8:9], v[2:3], off
	v_mov_b32_e32 v2, 0
	v_and_b32_e32 v1, 63, v0
	v_bfe_u32 v7, v0, 6, 1
	v_cmp_gt_u32_e32 vcc, 25, v10
	v_mov_b32_e32 v3, v2
	v_mov_b32_e32 v4, v2
	v_mov_b32_e32 v5, v2
	s_and_saveexec_b64 s[2:3], vcc
	s_cbranch_execz .LBB3_6
	v_lshrrev_b32_e32 v2, 5, v1
	v_lshl_or_b32 v2, v7, 1, v2
	s_waitcnt vmcnt(0)
	v_add_u32_e32 v13, v2, v8
	v_mov_b32_e32 v5, 0
	v_cmp_lt_i32_e32 vcc, v13, v9
	v_mov_b32_e32 v4, v5
	v_mov_b32_e32 v3, v5
	v_mov_b32_e32 v2, v5
	s_and_saveexec_b64 s[4:5], vcc
	s_cbranch_execz .LBB3_5
	s_load_dwordx2 s[6:7], s[0:1], 0x0
	v_lshlrev_b32_e32 v2, 4, v10
	v_mov_b32_e32 v3, 0
	s_movk_i32 s8, 0x190
	v_mad_i64_i32 v[4:5], s[8:9], v13, s8, v[2:3]
	s_waitcnt lgkmcnt(0)
	v_lshl_add_u64 v[4:5], s[6:7], 0, v[4:5]
	s_mov_b64 s[8:9], 0x960
	v_lshl_add_u64 v[10:11], v[4:5], 0, s[8:9]
	s_mov_b64 s[6:7], 0
	s_mov_b64 s[8:9], 0x1900
	v_mov_b32_e32 v2, v3
	v_mov_b32_e32 v4, v3
	v_mov_b32_e32 v5, v3
.LBB3_3:
	v_add_u32_e32 v30, 4, v13
	v_cmp_lt_i32_e64 s[10:11], v30, v9
	v_add_u32_e32 v30, 8, v13
	v_cmp_lt_i32_e64 s[12:13], v30, v9
	v_add_u32_e32 v30, 12, v13
	v_cmp_lt_i32_e64 s[14:15], v30, v9
	s_mov_b64 s[16:17], exec
	global_load_dwordx4 v[14:17], v[10:11], off offset:-2400
	s_and_b64 exec, s[16:17], s[10:11]
	s_cbranch_execz .Lpool_ld_done
	global_load_dwordx4 v[18:21], v[10:11], off offset:-800
	s_and_b64 exec, s[16:17], s[12:13]
	s_cbranch_execz .Lpool_ld_done
	global_load_dwordx4 v[22:25], v[10:11], off offset:800
	s_and_b64 exec, s[16:17], s[14:15]
	s_cbranch_execz .Lpool_ld_done
	global_load_dwordx4 v[26:29], v[10:11], off offset:2400
.Lpool_ld_done:
	s_mov_b64 exec, s[16:17]
	v_add_u32_e32 v13, 16, v13
	v_cmp_ge_i32_e32 vcc, v13, v9
	v_lshl_add_u64 v[10:11], v[10:11], 0, s[8:9]
	s_or_b64 s[6:7], vcc, s[6:7]
	s_waitcnt vmcnt(0)
	v_pk_add_f32 v[2:3], v[2:3], v[14:15]
	v_pk_add_f32 v[4:5], v[4:5], v[16:17]
	s_and_b64 exec, s[16:17], s[10:11]
	v_pk_add_f32 v[2:3], v[2:3], v[18:19]
	v_pk_add_f32 v[4:5], v[4:5], v[20:21]
	s_and_b64 exec, s[16:17], s[12:13]
	v_pk_add_f32 v[2:3], v[2:3], v[22:23]
	v_pk_add_f32 v[4:5], v[4:5], v[24:25]
	s_and_b64 exec, s[16:17], s[14:15]
	v_pk_add_f32 v[2:3], v[2:3], v[26:27]
	v_pk_add_f32 v[4:5], v[4:5], v[28:29]
	s_mov_b64 exec, s[16:17]
	s_andn2_b64 exec, exec, s[6:7]
	s_cbranch_execnz .LBB3_3
	s_or_b64 exec, exec, s[6:7]

	.amdhsa_kernel _Z11pool_kernelPKfPKiPDF16_
		.amdhsa_group_segment_fixed_size 1024
		.amdhsa_private_segment_fixed_size 0
		.amdhsa_kernarg_size 24
		.amdhsa_user_sgpr_count 2
		.amdhsa_user_sgpr_dispatch_ptr 0
		.amdhsa_user_sgpr_queue_ptr 0
		.amdhsa_user_sgpr_kernarg_segment_ptr 1
		.amdhsa_user_sgpr_dispatch_id 0
		.amdhsa_user_sgpr_kernarg_preload_length 0
		.amdhsa_user_sgpr_kernarg_preload_offset 0
		.amdhsa_user_sgpr_private_segment_size 0
		.amdhsa_uses_dynamic_stack 0
		.amdhsa_enable_private_segment 0
		.amdhsa_system_sgpr_workgroup_id_x 1
		.amdhsa_system_sgpr_workgroup_id_y 0
		.amdhsa_system_sgpr_workgroup_id_z 0
		.amdhsa_system_sgpr_workgroup_info 0
		.amdhsa_system_vgpr_workitem_id 0
		.amdhsa_next_free_vgpr 31
		.amdhsa_next_free_sgpr 20
		.amdhsa_accum_offset 32
		.amdhsa_reserve_vcc 1
		.amdhsa_float_round_mode_32 0
		.amdhsa_float_round_mode_16_64 0
		.amdhsa_float_denorm_mode_32 3
		.amdhsa_float_denorm_mode_16_64 3
		.amdhsa_dx10_clamp 1
		.amdhsa_ieee_mode 1
		.amdhsa_fp16_overflow 0
		.amdhsa_tg_split 0
		.amdhsa_exception_fp_ieee_invalid_op 0
		.amdhsa_exception_fp_denorm_src 0
		.amdhsa_exception_fp_ieee_div_zero 0
		.amdhsa_exception_fp_ieee_overflow 0
		.amdhsa_exception_fp_ieee_underflow 0
		.amdhsa_exception_fp_ieee_inexact 0
		.amdhsa_exception_int_div_zero 0
	.end_amdhsa_kernel

amdhsa.kernels:
  - .agpr_count:     0
    .args:
      - .actual_access:  read_only
        .address_space:  global
        .offset:         0
        .size:           8
        .value_kind:     global_buffer
      - .actual_access:  read_only
        .address_space:  global
        .offset:         8
        .size:           8
        .value_kind:     global_buffer
      - .actual_access:  read_only
        .address_space:  global
        .offset:         16
        .size:           8
        .value_kind:     global_buffer
      - .actual_access:  read_only
        .address_space:  global
        .offset:         24
        .size:           8
        .value_kind:     global_buffer
      - .actual_access:  read_only
        .address_space:  global
        .offset:         32
        .size:           8
        .value_kind:     global_buffer
      - .actual_access:  write_only
        .address_space:  global
        .offset:         40
        .size:           8
        .value_kind:     global_buffer
      - .actual_access:  write_only
        .address_space:  global
        .offset:         48
        .size:           8
        .value_kind:     global_buffer
      - .actual_access:  write_only
        .address_space:  global
        .offset:         56
        .size:           8
        .value_kind:     global_buffer
    .group_segment_fixed_size: 0
    .kernarg_segment_align: 8
    .kernarg_segment_size: 64
    .language:       OpenCL C
    .language_version:
      - 2
      - 0
    .max_flat_workgroup_size: 256
    .name:           _Z11prep_kernelPKfS0_S0_S0_S0_PDv8_DF16_S2_Pi
    .private_segment_fixed_size: 0
    .sgpr_count:     26
    .sgpr_spill_count: 0
    .symbol:         _Z11prep_kernelPKfS0_S0_S0_S0_PDv8_DF16_S2_Pi.kd
    .uniform_work_group_size: 1
    .uses_dynamic_stack: false
    .vgpr_count:     18
    .vgpr_spill_count: 0
    .wavefront_size: 64
  - .agpr_count:     0
    .args:
      - .actual_access:  read_only
        .address_space:  global
        .offset:         0
        .size:           8
        .value_kind:     global_buffer
      - .actual_access:  read_only
        .address_space:  global
        .offset:         8
        .size:           8
        .value_kind:     global_buffer
      - .actual_access:  read_only
        .address_space:  global
        .offset:         16
        .size:           8
        .value_kind:     global_buffer
      - .actual_access:  read_only
        .address_space:  global
        .offset:         24
        .size:           8
        .value_kind:     global_buffer
      - .actual_access:  read_only
        .address_space:  global
        .offset:         32
        .size:           8
        .value_kind:     global_buffer
      - .actual_access:  read_only
        .address_space:  global
        .offset:         40
        .size:           8
        .value_kind:     global_buffer
      - .actual_access:  read_only
        .address_space:  global
        .offset:         48
        .size:           8
        .value_kind:     global_buffer
      - .actual_access:  read_only
        .address_space:  global
        .offset:         56
        .size:           8
        .value_kind:     global_buffer
      - .actual_access:  read_only
        .address_space:  global
        .offset:         64
        .size:           8
        .value_kind:     global_buffer
      - .actual_access:  read_only
        .address_space:  global
        .offset:         72
        .size:           8
        .value_kind:     global_buffer
      - .actual_access:  read_only
        .address_space:  global
        .offset:         80
        .size:           8
        .value_kind:     global_buffer
      - .actual_access:  read_only
        .address_space:  global
        .offset:         88
        .size:           8
        .value_kind:     global_buffer
      - .actual_access:  read_only
        .address_space:  global
        .offset:         96
        .size:           8
        .value_kind:     global_buffer
      - .actual_access:  read_only
        .address_space:  global
        .offset:         104
        .size:           8
        .value_kind:     global_buffer
      - .actual_access:  write_only
        .address_space:  global
        .offset:         112
        .size:           8
        .value_kind:     global_buffer
      - .offset:         120
        .size:           4
        .value_kind:     by_value
      - .actual_access:  read_only
        .address_space:  global
        .offset:         128
        .size:           8
        .value_kind:     global_buffer
      - .actual_access:  read_only
        .address_space:  global
        .offset:         136
        .size:           8
        .value_kind:     global_buffer
      - .actual_access:  write_only
        .address_space:  global
        .offset:         144
        .size:           8
        .value_kind:     global_buffer
      - .actual_access:  read_only
        .address_space:  global
        .offset:         152
        .size:           8
        .value_kind:     global_buffer
      - .actual_access:  read_only
        .address_space:  global
        .offset:         160
        .size:           8
        .value_kind:     global_buffer
      - .address_space:  global
        .offset:         168
        .size:           8
        .value_kind:     global_buffer
      - .actual_access:  write_only
        .address_space:  global
        .offset:         176
        .size:           8
        .value_kind:     global_buffer
      - .address_space:  global
        .offset:         184
        .size:           8
        .value_kind:     global_buffer
      - .actual_access:  write_only
        .address_space:  global
        .offset:         192
        .size:           8
        .value_kind:     global_buffer
      - .actual_access:  write_only
        .address_space:  global
        .offset:         200
        .size:           8
        .value_kind:     global_buffer
    .group_segment_fixed_size: 21760
    .kernarg_segment_align: 8
    .kernarg_segment_size: 208
    .language:       OpenCL C
    .language_version:
      - 2
      - 0
    .max_flat_workgroup_size: 256
    .name:           _Z12embed_kernelPKiS0_S0_S0_S0_PKfS2_S2_S2_S2_S2_S2_S2_PKDv8_DF16_PfiS2_S2_PS3_S0_S0_PiS8_S8_P15HIP_vector_typeIiLj2EES8_
    .private_segment_fixed_size: 0
    .sgpr_count:     44
    .sgpr_spill_count: 0
    .symbol:         _Z12embed_kernelPKiS0_S0_S0_S0_PKfS2_S2_S2_S2_S2_S2_S2_PKDv8_DF16_PfiS2_S2_PS3_S0_S0_PiS8_S8_P15HIP_vector_typeIiLj2EES8_.kd
    .uniform_work_group_size: 1
    .uses_dynamic_stack: false
    .vgpr_count:     166
    .vgpr_spill_count: 0
    .wavefront_size: 64
  - .agpr_count:     0
    .args:
      - .actual_access:  read_only
        .address_space:  global
        .offset:         0
        .size:           8
        .value_kind:     global_buffer
      - .actual_access:  read_only
        .address_space:  global
        .offset:         8
        .size:           8
        .value_kind:     global_buffer
      - .actual_access:  read_only
        .address_space:  global
        .offset:         16
        .size:           8
        .value_kind:     global_buffer
      - .actual_access:  read_only
        .address_space:  global
        .offset:         24
        .size:           8
        .value_kind:     global_buffer
      - .actual_access:  read_only
        .address_space:  global
        .offset:         32
        .size:           8
        .value_kind:     global_buffer
      - .actual_access:  read_only
        .address_space:  global
        .offset:         40
        .size:           8
        .value_kind:     global_buffer
      - .actual_access:  read_only
        .address_space:  global
        .offset:         48
        .size:           8
        .value_kind:     global_buffer
      - .actual_access:  read_only
        .address_space:  global
        .offset:         56
        .size:           8
        .value_kind:     global_buffer
      - .actual_access:  write_only
        .address_space:  global
        .offset:         64
        .size:           8
        .value_kind:     global_buffer
      - .offset:         72
        .size:           4
        .value_kind:     by_value
    .group_segment_fixed_size: 30720
    .kernarg_segment_align: 8
    .kernarg_segment_size: 76
    .language:       OpenCL C
    .language_version:
      - 2
      - 0
    .max_flat_workgroup_size: 256
    .name:           _Z10gru_kernelPKfPKiS2_S2_PK15HIP_vector_typeIiLj2EEPKDv8_DF16_S0_S0_Pfi
    .private_segment_fixed_size: 0
    .sgpr_count:     31
    .sgpr_spill_count: 0
    .symbol:         _Z10gru_kernelPKfPKiS2_S2_PK15HIP_vector_typeIiLj2EEPKDv8_DF16_S0_S0_Pfi.kd
    .uniform_work_group_size: 1
    .uses_dynamic_stack: false
    .vgpr_count:     231
    .vgpr_spill_count: 0
    .wavefront_size: 64
  - .agpr_count:     0
    .args:
      - .actual_access:  read_only
        .address_space:  global
        .offset:         0
        .size:           8
        .value_kind:     global_buffer
      - .actual_access:  read_only
        .address_space:  global
        .offset:         8
        .size:           8
        .value_kind:     global_buffer
      - .actual_access:  write_only
        .address_space:  global
        .offset:         16
        .size:           8
        .value_kind:     global_buffer
    .group_segment_fixed_size: 1024
    .kernarg_segment_align: 8
    .kernarg_segment_size: 24
    .language:       OpenCL C
    .language_version:
      - 2
      - 0
    .max_flat_workgroup_size: 256
    .name:           _Z11pool_kernelPKfPKiPDF16_
    .private_segment_fixed_size: 0
    .sgpr_count:     26
    .sgpr_spill_count: 0
    .symbol:         _Z11pool_kernelPKfPKiPDF16_.kd
    .uniform_work_group_size: 1
    .uses_dynamic_stack: false
    .vgpr_count:     31
    .vgpr_spill_count: 0
    .wavefront_size: 64
  - .agpr_count:     0
    .args:
      - .actual_access:  read_only
        .address_space:  global
        .offset:         0
        .size:           8
        .value_kind:     global_buffer
      - .actual_access:  read_only
        .address_space:  global
        .offset:         8
        .size:           8
        .value_kind:     global_buffer
      - .actual_access:  write_only
        .address_space:  global
        .offset:         16
        .size:           8
        .value_kind:     global_buffer
    .group_segment_fixed_size: 90112
    .kernarg_segment_align: 8
    .kernarg_segment_size: 24
    .language:       OpenCL C
    .language_version:
      - 2
      - 0
    .max_flat_workgroup_size: 256
    .name:           _Z9fc_kernelPKDv8_DF16_S1_Pf
    .private_segment_fixed_size: 0
    .sgpr_count:     17
    .sgpr_spill_count: 0
    .symbol:         _Z9fc_kernelPKDv8_DF16_S1_Pf.kd
    .uniform_work_group_size: 1
    .uses_dynamic_stack: false
    .vgpr_count:     208
    .vgpr_spill_count: 0
    .wavefront_size: 64
